# layer-0 MFMAs of the second tile pair issued two per relu/cvt group instead of trailing
# speedup vs baseline: 1.0041x; 1.0041x over previous
.LBB1_4:
	s_and_saveexec_b64 s[8:9], s[2:3]
	v_perm_b32 v5, v1, v102, s23
	v_perm_b32 v9, v121, v103, s23
	v_perm_b32 v17, v144, v115, s23
	v_perm_b32 v29, v145, v116, s23
	s_or_b64 exec, exec, s[8:9]
	v_mfma_f32_16x16x32_f16 v[164:167], v[30:33], v[2:5], 0
	v_mfma_f32_16x16x32_f16 v[180:183], v[22:25], v[2:5], 0
	s_cmp_lg_u32 s22, 0x818000
	v_mfma_f32_16x16x32_f16 v[168:171], v[30:33], v[6:9], 0
	v_mfma_f32_16x16x32_f16 v[184:187], v[22:25], v[6:9], 0
	s_cselect_b32 s9, s11, 15
	v_mfma_f32_16x16x32_f16 v[172:175], v[30:33], v[14:17], 0
	v_mfma_f32_16x16x32_f16 v[188:191], v[22:25], v[14:17], 0
	v_mfma_f32_16x16x32_f16 v[176:179], v[30:33], v[26:29], 0
	v_mfma_f32_16x16x32_f16 v[192:195], v[22:25], v[26:29], 0
	v_mfma_f32_16x16x32_f16 v[208:211], v[18:21], v[2:5], 0
	v_mfma_f32_16x16x32_f16 v[224:227], v[10:13], v[2:5], 0
	v_cvt_pk_f16_f32 v122, v164, v165
	v_cvt_pk_f16_f32 v123, v166, v167
	v_pk_max_f16 v122, v122, 0
	v_pk_max_f16 v123, v123, 0
	v_cvt_pk_f16_f32 v124, v180, v181
	v_cvt_pk_f16_f32 v125, v182, v183
	v_pk_max_f16 v124, v124, 0
	v_pk_max_f16 v125, v125, 0
	ds_write_b128 v107, v[122:125]
	v_mfma_f32_16x16x32_f16 v[212:215], v[18:21], v[6:9], 0
	v_mfma_f32_16x16x32_f16 v[228:231], v[10:13], v[6:9], 0
	v_cvt_pk_f16_f32 v126, v168, v169
	v_cvt_pk_f16_f32 v127, v170, v171
	v_pk_max_f16 v126, v126, 0
	v_pk_max_f16 v127, v127, 0
	v_cvt_pk_f16_f32 v128, v184, v185
	v_cvt_pk_f16_f32 v129, v186, v187
	v_pk_max_f16 v128, v128, 0
	v_pk_max_f16 v129, v129, 0
	ds_write_b128 v107, v[126:129] offset:16384
	v_mfma_f32_16x16x32_f16 v[216:219], v[18:21], v[14:17], 0
	v_mfma_f32_16x16x32_f16 v[232:235], v[10:13], v[14:17], 0
	v_cvt_pk_f16_f32 v134, v172, v173
	v_cvt_pk_f16_f32 v135, v174, v175
	v_pk_max_f16 v134, v134, 0
	v_pk_max_f16 v135, v135, 0
	v_cvt_pk_f16_f32 v136, v188, v189
	v_cvt_pk_f16_f32 v137, v190, v191
	v_pk_max_f16 v136, v136, 0
	v_pk_max_f16 v137, v137, 0
	ds_write_b128 v107, v[134:137] offset:32768
	v_mfma_f32_16x16x32_f16 v[220:223], v[18:21], v[26:29], 0
	v_mfma_f32_16x16x32_f16 v[236:239], v[10:13], v[26:29], 0
	v_cvt_pk_f16_f32 v138, v176, v177
	v_cvt_pk_f16_f32 v139, v178, v179
	v_pk_max_f16 v138, v138, 0
	v_pk_max_f16 v139, v139, 0
	v_cvt_pk_f16_f32 v140, v192, v193
	v_cvt_pk_f16_f32 v141, v194, v195
	v_pk_max_f16 v140, v140, 0
	v_pk_max_f16 v141, v141, 0
	ds_write_b128 v107, v[138:141] offset:49152
	v_add_u32_e32 v111, s64, v111
	v_add_u32_e32 v98, s65, v98
	s_lshl_b32 s20, s9, 7
	v_lshl_add_u64 v[0:1], s[20:21], 3, v[132:133]
	s_add_i32 s25, s22, s34
	s_lshl_b32 s8, s9, 8
	buffer_load_dwordx4 v[192:195], v147, s[16:19], s25 offen
	buffer_load_dwordx4 v[196:199], v148, s[16:19], s25 offen
	buffer_load_dwordx4 v[200:203], v149, s[16:19], s25 offen
	buffer_load_dwordx4 v[204:207], v150, s[16:19], s25 offen
	s_waitcnt vmcnt(19)
	v_mfma_f32_16x16x32_f16 v[164:167], v[58:61], v[122:125], v[240:243]
	v_cvt_pk_f16_f32 v142, v208, v209
	v_cvt_pk_f16_f32 v143, v210, v211
	v_mfma_f32_16x16x32_f16 v[168:171], v[58:61], v[126:129], v[240:243]
	v_pk_max_f16 v142, v142, 0
	v_pk_max_f16 v143, v143, 0
	v_mfma_f32_16x16x32_f16 v[172:175], v[58:61], v[134:137], v[240:243]
	v_cvt_pk_f16_f32 v144, v224, v225
	v_cvt_pk_f16_f32 v145, v226, v227
	v_mfma_f32_16x16x32_f16 v[10:13], v[58:61], v[138:141], v[240:243]
	v_pk_max_f16 v144, v144, 0
	v_pk_max_f16 v145, v145, 0
	ds_write_b128 v108, v[142:145]
	s_waitcnt vmcnt(18)
	v_mfma_f32_16x16x32_f16 v[58:61], v[54:57], v[122:125], v[244:247]
	v_cvt_pk_f16_f32 v152, v212, v213
	v_cvt_pk_f16_f32 v153, v214, v215
	v_mfma_f32_16x16x32_f16 v[176:179], v[54:57], v[126:129], v[244:247]
	v_pk_max_f16 v152, v152, 0
	v_pk_max_f16 v153, v153, 0
	v_mfma_f32_16x16x32_f16 v[180:183], v[54:57], v[134:137], v[244:247]
	v_cvt_pk_f16_f32 v154, v228, v229
	v_cvt_pk_f16_f32 v155, v230, v231
	v_mfma_f32_16x16x32_f16 v[18:21], v[54:57], v[138:141], v[244:247]
	v_pk_max_f16 v154, v154, 0
	v_pk_max_f16 v155, v155, 0
	ds_write_b128 v108, v[152:155] offset:16384
	s_waitcnt vmcnt(17)
	v_mfma_f32_16x16x32_f16 v[54:57], v[50:53], v[122:125], v[248:251]
	v_cvt_pk_f16_f32 v156, v216, v217
	v_cvt_pk_f16_f32 v157, v218, v219
	v_mfma_f32_16x16x32_f16 v[184:187], v[50:53], v[126:129], v[248:251]
	v_pk_max_f16 v156, v156, 0
	v_pk_max_f16 v157, v157, 0
	v_mfma_f32_16x16x32_f16 v[188:191], v[50:53], v[134:137], v[248:251]
	v_cvt_pk_f16_f32 v158, v232, v233
	v_cvt_pk_f16_f32 v159, v234, v235
	v_mfma_f32_16x16x32_f16 v[22:25], v[50:53], v[138:141], v[248:251]
	v_pk_max_f16 v158, v158, 0
	v_pk_max_f16 v159, v159, 0
	ds_write_b128 v108, v[156:159] offset:32768
	s_waitcnt vmcnt(16)
	v_mfma_f32_16x16x32_f16 v[50:53], v[38:41], v[122:125], v[252:255]
	v_cvt_pk_f16_f32 v160, v220, v221
	v_cvt_pk_f16_f32 v161, v222, v223
	v_mfma_f32_16x16x32_f16 v[122:125], v[38:41], v[126:129], v[252:255]
	v_pk_max_f16 v160, v160, 0
	v_pk_max_f16 v161, v161, 0
	v_mfma_f32_16x16x32_f16 v[126:129], v[38:41], v[134:137], v[252:255]
	v_cvt_pk_f16_f32 v162, v236, v237
	v_cvt_pk_f16_f32 v163, v238, v239
	v_mfma_f32_16x16x32_f16 v[38:41], v[38:41], v[138:141], v[252:255]
	v_pk_max_f16 v162, v162, 0
	v_pk_max_f16 v163, v163, 0
	ds_write_b128 v108, v[160:163] offset:49152
	s_add_i32 s9, s22, s35
	s_waitcnt vmcnt(15)
	v_mfma_f32_16x16x32_f16 v[164:167], v[94:97], v[142:145], v[164:167]
	v_mfma_f32_16x16x32_f16 v[168:171], v[94:97], v[152:155], v[168:171]
	s_waitcnt vmcnt(14)
	v_mfma_f32_16x16x32_f16 v[58:61], v[90:93], v[142:145], v[58:61]
	v_mfma_f32_16x16x32_f16 v[176:179], v[90:93], v[152:155], v[176:179]
	s_waitcnt vmcnt(13)
	v_mfma_f32_16x16x32_f16 v[54:57], v[78:81], v[142:145], v[54:57]
	v_mfma_f32_16x16x32_f16 v[184:187], v[78:81], v[152:155], v[184:187]
	s_waitcnt vmcnt(12)
	v_mfma_f32_16x16x32_f16 v[50:53], v[34:37], v[142:145], v[50:53]
	buffer_load_dwordx4 v[140:143], v147, s[16:19], s9 offen
	buffer_load_dwordx4 v[220:223], v148, s[16:19], s9 offen
	v_mfma_f32_16x16x32_f16 v[122:125], v[34:37], v[152:155], v[122:125]
	buffer_load_dwordx4 v[152:155], v149, s[16:19], s9 offen
	buffer_load_dwordx4 v[224:227], v150, s[16:19], s9 offen
	s_mov_b32 s9, s21
	s_waitcnt lgkmcnt(0)
	s_barrier
	v_add_u32_e32 v99, s66, v99
	ds_read_b128 v[136:139], v99
	ds_read_b128 v[208:211], v99 offset:16384
	ds_read_b128 v[212:215], v99 offset:32768
	ds_read_b128 v[216:219], v99 offset:49152
	v_mfma_f32_16x16x32_f16 v[172:175], v[94:97], v[156:159], v[172:175]
	v_mfma_f32_16x16x32_f16 v[94:97], v[94:97], v[160:163], v[10:13]
	s_nop 2
	v_lshl_add_u64 v[10:11], s[8:9], 4, v[130:131]
	v_mfma_f32_16x16x32_f16 v[180:183], v[90:93], v[156:159], v[180:183]
	v_mfma_f32_16x16x32_f16 v[90:93], v[90:93], v[160:163], v[18:21]
	v_mfma_f32_16x16x32_f16 v[188:191], v[78:81], v[156:159], v[188:191]
	v_mfma_f32_16x16x32_f16 v[78:81], v[78:81], v[160:163], v[22:25]
	global_load_dwordx4 v[30:33], v[10:11], off
	s_nop 1
	global_load_dwordx4 v[22:25], v[10:11], off offset:1024
	global_load_dwordx4 v[18:21], v[10:11], off offset:2048
	s_nop 0
	global_load_dwordx4 v[10:13], v[10:11], off offset:3072
	s_nop 0
	global_load_dwordx2 v[134:135], v[0:1], off
	v_mfma_f32_16x16x32_f16 v[126:129], v[34:37], v[156:159], v[126:129]
	v_mfma_f32_16x16x32_f16 v[34:37], v[34:37], v[160:163], v[38:41]
	s_nop 2
	v_add_u32_e32 v100, s67, v100
	ds_read_b128 v[38:41], v100
	ds_read_b128 v[156:159], v100 offset:16384
	ds_read_b128 v[160:163], v100 offset:32768
	ds_read_b128 v[228:231], v100 offset:49152
	s_add_i32 s8, s22, s36
	s_waitcnt vmcnt(20) lgkmcnt(7)
	v_mfma_f32_16x16x32_f16 v[164:167], v[82:85], v[136:139], v[164:167]
	s_waitcnt lgkmcnt(6)
	v_mfma_f32_16x16x32_f16 v[168:171], v[82:85], v[208:211], v[168:171]
	s_waitcnt lgkmcnt(5)
	v_mfma_f32_16x16x32_f16 v[172:175], v[82:85], v[212:215], v[172:175]
	s_waitcnt lgkmcnt(4)
	v_mfma_f32_16x16x32_f16 v[82:85], v[82:85], v[216:219], v[94:97]
	s_waitcnt vmcnt(19)
	v_mfma_f32_16x16x32_f16 v[58:61], v[70:73], v[136:139], v[58:61]
	v_mfma_f32_16x16x32_f16 v[94:97], v[70:73], v[208:211], v[176:179]
	v_mfma_f32_16x16x32_f16 v[176:179], v[70:73], v[212:215], v[180:183]
	v_mfma_f32_16x16x32_f16 v[70:73], v[70:73], v[216:219], v[90:93]
	s_waitcnt vmcnt(18)
	v_mfma_f32_16x16x32_f16 v[54:57], v[62:65], v[136:139], v[54:57]
	v_mfma_f32_16x16x32_f16 v[90:93], v[62:65], v[208:211], v[184:187]
	v_mfma_f32_16x16x32_f16 v[180:183], v[62:65], v[212:215], v[188:191]
	v_mfma_f32_16x16x32_f16 v[62:65], v[62:65], v[216:219], v[78:81]
	s_waitcnt vmcnt(17)
	v_mfma_f32_16x16x32_f16 v[50:53], v[42:45], v[136:139], v[50:53]
	v_mfma_f32_16x16x32_f16 v[78:81], v[42:45], v[208:211], v[122:125]
	v_mfma_f32_16x16x32_f16 v[122:125], v[42:45], v[212:215], v[126:129]
	s_nop 2
	buffer_load_dwordx4 v[126:129], v147, s[16:19], s8 offen
	buffer_load_dwordx4 v[136:139], v148, s[16:19], s8 offen
	buffer_load_dwordx4 v[184:187], v149, s[16:19], s8 offen
	buffer_load_dwordx4 v[188:191], v150, s[16:19], s8 offen
	v_mfma_f32_16x16x32_f16 v[34:37], v[42:45], v[216:219], v[34:37]
	v_add_u32_e32 v111, s68, v111
	ds_read_b128 v[42:45], v111
	ds_read_b128 v[208:211], v111 offset:16384
	ds_read_b128 v[212:215], v111 offset:32768
	ds_read_b128 v[216:219], v111 offset:49152
	s_add_i32 s8, s22, s37
	s_waitcnt vmcnt(20) lgkmcnt(7)
	v_mfma_f32_16x16x32_f16 v[164:167], v[86:89], v[38:41], v[164:167]
	s_waitcnt lgkmcnt(6)
	v_mfma_f32_16x16x32_f16 v[168:171], v[86:89], v[156:159], v[168:171]
	s_waitcnt lgkmcnt(5)
	v_mfma_f32_16x16x32_f16 v[172:175], v[86:89], v[160:163], v[172:175]
	s_waitcnt lgkmcnt(4)
	v_mfma_f32_16x16x32_f16 v[82:85], v[86:89], v[228:231], v[82:85]
	s_waitcnt vmcnt(19)
	v_mfma_f32_16x16x32_f16 v[58:61], v[74:77], v[38:41], v[58:61]
	v_mfma_f32_16x16x32_f16 v[86:89], v[74:77], v[156:159], v[94:97]
	v_mfma_f32_16x16x32_f16 v[94:97], v[74:77], v[160:163], v[176:179]
	v_mfma_f32_16x16x32_f16 v[70:73], v[74:77], v[228:231], v[70:73]
	s_waitcnt vmcnt(18)
	v_mfma_f32_16x16x32_f16 v[54:57], v[66:69], v[38:41], v[54:57]
	v_mfma_f32_16x16x32_f16 v[74:77], v[66:69], v[156:159], v[90:93]
	v_mfma_f32_16x16x32_f16 v[90:93], v[66:69], v[160:163], v[180:183]
	v_mfma_f32_16x16x32_f16 v[62:65], v[66:69], v[228:231], v[62:65]
	s_waitcnt vmcnt(17)
	v_mfma_f32_16x16x32_f16 v[38:41], v[46:49], v[38:41], v[50:53]
	v_mfma_f32_16x16x32_f16 v[50:53], v[46:49], v[156:159], v[78:81]
	v_mfma_f32_16x16x32_f16 v[66:69], v[46:49], v[160:163], v[122:125]
	s_nop 1
	buffer_load_dwordx4 v[78:81], v147, s[16:19], s8 offen
	buffer_load_dwordx4 v[122:125], v148, s[16:19], s8 offen
	buffer_load_dwordx4 v[156:159], v149, s[16:19], s8 offen
	buffer_load_dwordx4 v[160:163], v150, s[16:19], s8 offen
	v_mfma_f32_16x16x32_f16 v[34:37], v[46:49], v[228:231], v[34:37]
	v_add_u32_e32 v98, s69, v98
	ds_read_b128 v[46:49], v98
	ds_read_b128 v[176:179], v98 offset:16384
	ds_read_b128 v[180:183], v98 offset:32768
	ds_read_b128 v[228:231], v98 offset:49152
	s_add_i32 s8, s22, s38
	s_waitcnt vmcnt(20) lgkmcnt(7)
	v_mfma_f32_16x16x32_f16 v[164:167], v[192:195], v[42:45], v[164:167]
	s_waitcnt lgkmcnt(6)
	v_mfma_f32_16x16x32_f16 v[168:171], v[192:195], v[208:211], v[168:171]
	s_waitcnt lgkmcnt(5)
	v_mfma_f32_16x16x32_f16 v[172:175], v[192:195], v[212:215], v[172:175]
	s_waitcnt lgkmcnt(4)
	v_mfma_f32_16x16x32_f16 v[82:85], v[192:195], v[216:219], v[82:85]
	s_waitcnt vmcnt(19)
	v_mfma_f32_16x16x32_f16 v[58:61], v[196:199], v[42:45], v[58:61]
	v_mfma_f32_16x16x32_f16 v[86:89], v[196:199], v[208:211], v[86:89]
	v_mfma_f32_16x16x32_f16 v[94:97], v[196:199], v[212:215], v[94:97]
	v_mfma_f32_16x16x32_f16 v[70:73], v[196:199], v[216:219], v[70:73]
	s_waitcnt vmcnt(18)
	v_mfma_f32_16x16x32_f16 v[54:57], v[200:203], v[42:45], v[54:57]
	v_mfma_f32_16x16x32_f16 v[74:77], v[200:203], v[208:211], v[74:77]
	v_mfma_f32_16x16x32_f16 v[90:93], v[200:203], v[212:215], v[90:93]
	v_mfma_f32_16x16x32_f16 v[62:65], v[200:203], v[216:219], v[62:65]
	s_waitcnt vmcnt(17)
	v_mfma_f32_16x16x32_f16 v[38:41], v[204:207], v[42:45], v[38:41]
	v_mfma_f32_16x16x32_f16 v[42:45], v[204:207], v[208:211], v[50:53]
	v_mfma_f32_16x16x32_f16 v[50:53], v[204:207], v[212:215], v[66:69]
	s_nop 2
	buffer_load_dwordx4 v[66:69], v147, s[16:19], s8 offen
	buffer_load_dwordx4 v[192:195], v148, s[16:19], s8 offen
	buffer_load_dwordx4 v[196:199], v149, s[16:19], s8 offen
	buffer_load_dwordx4 v[200:203], v150, s[16:19], s8 offen
	v_mfma_f32_16x16x32_f16 v[34:37], v[204:207], v[216:219], v[34:37]
	v_add_u32_e32 v99, s70, v99
	ds_read_b128 v[204:207], v99
	ds_read_b128 v[208:211], v99 offset:16384
	ds_read_b128 v[212:215], v99 offset:32768
	ds_read_b128 v[216:219], v99 offset:49152
	s_add_i32 s8, s22, s39
	s_waitcnt vmcnt(20) lgkmcnt(7)
	v_mfma_f32_16x16x32_f16 v[164:167], v[140:143], v[46:49], v[164:167]
	s_waitcnt lgkmcnt(6)
	v_mfma_f32_16x16x32_f16 v[168:171], v[140:143], v[176:179], v[168:171]
	s_waitcnt lgkmcnt(5)
	v_mfma_f32_16x16x32_f16 v[172:175], v[140:143], v[180:183], v[172:175]
	s_waitcnt lgkmcnt(4)
	v_mfma_f32_16x16x32_f16 v[82:85], v[140:143], v[228:231], v[82:85]
	s_waitcnt vmcnt(19)
	v_mfma_f32_16x16x32_f16 v[58:61], v[220:223], v[46:49], v[58:61]
	v_mfma_f32_16x16x32_f16 v[86:89], v[220:223], v[176:179], v[86:89]
	s_waitcnt vmcnt(18)
	v_mfma_f32_16x16x32_f16 v[54:57], v[152:155], v[46:49], v[54:57]
	v_mfma_f32_16x16x32_f16 v[74:77], v[152:155], v[176:179], v[74:77]
	v_mfma_f32_16x16x32_f16 v[90:93], v[152:155], v[180:183], v[90:93]
	v_mfma_f32_16x16x32_f16 v[62:65], v[152:155], v[228:231], v[62:65]
	s_waitcnt vmcnt(17)
	v_mfma_f32_16x16x32_f16 v[38:41], v[224:227], v[46:49], v[38:41]
	v_mfma_f32_16x16x32_f16 v[42:45], v[224:227], v[176:179], v[42:45]
	v_mfma_f32_16x16x32_f16 v[46:49], v[224:227], v[180:183], v[50:53]
	s_nop 2
	buffer_load_dwordx4 v[50:53], v147, s[16:19], s8 offen
	buffer_load_dwordx4 v[140:143], v148, s[16:19], s8 offen
	buffer_load_dwordx4 v[152:155], v149, s[16:19], s8 offen
	buffer_load_dwordx4 v[176:179], v150, s[16:19], s8 offen
	v_mfma_f32_16x16x32_f16 v[94:97], v[220:223], v[180:183], v[94:97]
	v_mfma_f32_16x16x32_f16 v[70:73], v[220:223], v[228:231], v[70:73]
	v_mfma_f32_16x16x32_f16 v[34:37], v[224:227], v[228:231], v[34:37]
	v_add_u32_e32 v100, s71, v100
	ds_read_b128 v[180:183], v100
	ds_read_b128 v[220:223], v100 offset:16384
	ds_read_b128 v[224:227], v100 offset:32768
	ds_read_b128 v[228:231], v100 offset:49152
	s_add_i32 s8, s22, s40
	s_waitcnt vmcnt(15) lgkmcnt(7)
	v_mfma_f32_16x16x32_f16 v[164:167], v[126:129], v[204:207], v[164:167]
	s_waitcnt lgkmcnt(6)
	v_mfma_f32_16x16x32_f16 v[168:171], v[126:129], v[208:211], v[168:171]
	s_waitcnt lgkmcnt(5)
	v_mfma_f32_16x16x32_f16 v[172:175], v[126:129], v[212:215], v[172:175]
	s_waitcnt lgkmcnt(4)
	v_mfma_f32_16x16x32_f16 v[82:85], v[126:129], v[216:219], v[82:85]
	s_waitcnt vmcnt(14)
	v_mfma_f32_16x16x32_f16 v[58:61], v[136:139], v[204:207], v[58:61]
	v_mfma_f32_16x16x32_f16 v[86:89], v[136:139], v[208:211], v[86:89]
	v_mfma_f32_16x16x32_f16 v[94:97], v[136:139], v[212:215], v[94:97]
	v_mfma_f32_16x16x32_f16 v[70:73], v[136:139], v[216:219], v[70:73]
	s_waitcnt vmcnt(13)
	v_mfma_f32_16x16x32_f16 v[54:57], v[184:187], v[204:207], v[54:57]
	v_mfma_f32_16x16x32_f16 v[74:77], v[184:187], v[208:211], v[74:77]
	v_mfma_f32_16x16x32_f16 v[90:93], v[184:187], v[212:215], v[90:93]
	v_mfma_f32_16x16x32_f16 v[62:65], v[184:187], v[216:219], v[62:65]
	s_waitcnt vmcnt(12)
	v_mfma_f32_16x16x32_f16 v[38:41], v[188:191], v[204:207], v[38:41]
	buffer_load_dwordx4 v[126:129], v147, s[16:19], s8 offen
	buffer_load_dwordx4 v[136:139], v148, s[16:19], s8 offen
	buffer_load_dwordx4 v[184:187], v149, s[16:19], s8 offen
	buffer_load_dwordx4 v[204:207], v150, s[16:19], s8 offen
	v_mfma_f32_16x16x32_f16 v[42:45], v[188:191], v[208:211], v[42:45]
	v_mfma_f32_16x16x32_f16 v[46:49], v[188:191], v[212:215], v[46:49]
	v_mfma_f32_16x16x32_f16 v[34:37], v[188:191], v[216:219], v[34:37]
	v_add_u32_e32 v111, s72, v111
	ds_read_b128 v[188:191], v111
	ds_read_b128 v[208:211], v111 offset:16384
	ds_read_b128 v[212:215], v111 offset:32768
	ds_read_b128 v[216:219], v111 offset:49152
	s_add_i32 s8, s22, s41
	s_waitcnt vmcnt(15) lgkmcnt(7)
	v_mfma_f32_16x16x32_f16 v[164:167], v[78:81], v[180:183], v[164:167]
	s_waitcnt lgkmcnt(6)
	v_mfma_f32_16x16x32_f16 v[168:171], v[78:81], v[220:223], v[168:171]
	s_waitcnt lgkmcnt(5)
	v_mfma_f32_16x16x32_f16 v[172:175], v[78:81], v[224:227], v[172:175]
	s_waitcnt lgkmcnt(4)
	v_mfma_f32_16x16x32_f16 v[78:81], v[78:81], v[228:231], v[82:85]
	s_waitcnt vmcnt(14)
	v_mfma_f32_16x16x32_f16 v[58:61], v[122:125], v[180:183], v[58:61]
	v_mfma_f32_16x16x32_f16 v[82:85], v[122:125], v[220:223], v[86:89]
	v_mfma_f32_16x16x32_f16 v[86:89], v[122:125], v[224:227], v[94:97]
	v_mfma_f32_16x16x32_f16 v[70:73], v[122:125], v[228:231], v[70:73]
	s_waitcnt vmcnt(13)
	v_mfma_f32_16x16x32_f16 v[54:57], v[156:159], v[180:183], v[54:57]
	v_mfma_f32_16x16x32_f16 v[74:77], v[156:159], v[220:223], v[74:77]
	v_mfma_f32_16x16x32_f16 v[90:93], v[156:159], v[224:227], v[90:93]
	v_mfma_f32_16x16x32_f16 v[62:65], v[156:159], v[228:231], v[62:65]
	s_waitcnt vmcnt(12)
	v_mfma_f32_16x16x32_f16 v[38:41], v[160:163], v[180:183], v[38:41]
	buffer_load_dwordx4 v[94:97], v147, s[16:19], s8 offen
	buffer_load_dwordx4 v[122:125], v148, s[16:19], s8 offen
	buffer_load_dwordx4 v[156:159], v149, s[16:19], s8 offen
	buffer_load_dwordx4 v[180:183], v150, s[16:19], s8 offen
	v_mfma_f32_16x16x32_f16 v[42:45], v[160:163], v[220:223], v[42:45]
	v_mfma_f32_16x16x32_f16 v[46:49], v[160:163], v[224:227], v[46:49]
	v_mfma_f32_16x16x32_f16 v[34:37], v[160:163], v[228:231], v[34:37]
	v_add_u32_e32 v98, s73, v98
	ds_read_b128 v[160:163], v98
	ds_read_b128 v[220:223], v98 offset:16384
	ds_read_b128 v[224:227], v98 offset:32768
	ds_read_b128 v[228:231], v98 offset:49152
	s_add_i32 s8, s22, s42
	s_waitcnt vmcnt(15) lgkmcnt(7)
	v_mfma_f32_16x16x32_f16 v[164:167], v[66:69], v[188:191], v[164:167]
	s_waitcnt lgkmcnt(6)
	v_mfma_f32_16x16x32_f16 v[168:171], v[66:69], v[208:211], v[168:171]
	s_waitcnt lgkmcnt(5)
	v_mfma_f32_16x16x32_f16 v[172:175], v[66:69], v[212:215], v[172:175]
	s_waitcnt lgkmcnt(4)
	v_mfma_f32_16x16x32_f16 v[66:69], v[66:69], v[216:219], v[78:81]
	s_waitcnt vmcnt(14)
	v_mfma_f32_16x16x32_f16 v[58:61], v[192:195], v[188:191], v[58:61]
	v_mfma_f32_16x16x32_f16 v[78:81], v[192:195], v[208:211], v[82:85]
	v_mfma_f32_16x16x32_f16 v[82:85], v[192:195], v[212:215], v[86:89]
	v_mfma_f32_16x16x32_f16 v[70:73], v[192:195], v[216:219], v[70:73]
	s_waitcnt vmcnt(13)
	v_mfma_f32_16x16x32_f16 v[54:57], v[196:199], v[188:191], v[54:57]
	v_mfma_f32_16x16x32_f16 v[74:77], v[196:199], v[208:211], v[74:77]
	v_mfma_f32_16x16x32_f16 v[86:89], v[196:199], v[212:215], v[90:93]
	v_mfma_f32_16x16x32_f16 v[62:65], v[196:199], v[216:219], v[62:65]
	s_waitcnt vmcnt(12)
	v_mfma_f32_16x16x32_f16 v[38:41], v[200:203], v[188:191], v[38:41]
	buffer_load_dwordx4 v[90:93], v147, s[16:19], s8 offen
	buffer_load_dwordx4 v[188:191], v148, s[16:19], s8 offen
	buffer_load_dwordx4 v[192:195], v149, s[16:19], s8 offen
	buffer_load_dwordx4 v[196:199], v150, s[16:19], s8 offen
	v_mfma_f32_16x16x32_f16 v[42:45], v[200:203], v[208:211], v[42:45]
	v_mfma_f32_16x16x32_f16 v[46:49], v[200:203], v[212:215], v[46:49]
	v_mfma_f32_16x16x32_f16 v[34:37], v[200:203], v[216:219], v[34:37]
	v_add_u32_e32 v99, s74, v99
	ds_read_b128 v[200:203], v99
	ds_read_b128 v[208:211], v99 offset:16384
	ds_read_b128 v[212:215], v99 offset:32768
	ds_read_b128 v[216:219], v99 offset:49152
	s_add_i32 s8, s22, s43
	s_waitcnt vmcnt(15) lgkmcnt(7)
	v_mfma_f32_16x16x32_f16 v[164:167], v[50:53], v[160:163], v[164:167]
	s_waitcnt lgkmcnt(6)
	v_mfma_f32_16x16x32_f16 v[168:171], v[50:53], v[220:223], v[168:171]
	s_waitcnt lgkmcnt(5)
	v_mfma_f32_16x16x32_f16 v[172:175], v[50:53], v[224:227], v[172:175]
	s_waitcnt lgkmcnt(4)
	v_mfma_f32_16x16x32_f16 v[50:53], v[50:53], v[228:231], v[66:69]
	s_waitcnt vmcnt(14)
	v_mfma_f32_16x16x32_f16 v[58:61], v[140:143], v[160:163], v[58:61]
	v_mfma_f32_16x16x32_f16 v[66:69], v[140:143], v[220:223], v[78:81]
	v_mfma_f32_16x16x32_f16 v[78:81], v[140:143], v[224:227], v[82:85]
	v_mfma_f32_16x16x32_f16 v[70:73], v[140:143], v[228:231], v[70:73]
	s_waitcnt vmcnt(13)
	v_mfma_f32_16x16x32_f16 v[54:57], v[152:155], v[160:163], v[54:57]
	v_mfma_f32_16x16x32_f16 v[74:77], v[152:155], v[220:223], v[74:77]
	v_mfma_f32_16x16x32_f16 v[82:85], v[152:155], v[224:227], v[86:89]
	v_mfma_f32_16x16x32_f16 v[62:65], v[152:155], v[228:231], v[62:65]
	s_waitcnt vmcnt(12)
	v_mfma_f32_16x16x32_f16 v[38:41], v[176:179], v[160:163], v[38:41]
	buffer_load_dwordx4 v[86:89], v147, s[16:19], s8 offen
	buffer_load_dwordx4 v[140:143], v148, s[16:19], s8 offen
	buffer_load_dwordx4 v[152:155], v149, s[16:19], s8 offen
	buffer_load_dwordx4 v[160:163], v150, s[16:19], s8 offen
	v_mfma_f32_16x16x32_f16 v[42:45], v[176:179], v[220:223], v[42:45]
	v_mfma_f32_16x16x32_f16 v[46:49], v[176:179], v[224:227], v[46:49]
	v_mfma_f32_16x16x32_f16 v[34:37], v[176:179], v[228:231], v[34:37]
	v_add_u32_e32 v100, s75, v100
	ds_read_b128 v[176:179], v100
	ds_read_b128 v[220:223], v100 offset:16384
	ds_read_b128 v[224:227], v100 offset:32768
	ds_read_b128 v[228:231], v100 offset:49152
	s_add_i32 s8, s22, s44
	s_waitcnt vmcnt(15) lgkmcnt(7)
	v_mfma_f32_16x16x32_f16 v[164:167], v[126:129], v[200:203], v[164:167]
	s_waitcnt lgkmcnt(6)
	v_mfma_f32_16x16x32_f16 v[168:171], v[126:129], v[208:211], v[168:171]
	s_waitcnt lgkmcnt(5)
	v_mfma_f32_16x16x32_f16 v[172:175], v[126:129], v[212:215], v[172:175]
	s_waitcnt lgkmcnt(4)
	v_mfma_f32_16x16x32_f16 v[50:53], v[126:129], v[216:219], v[50:53]
	s_waitcnt vmcnt(14)
	v_mfma_f32_16x16x32_f16 v[58:61], v[136:139], v[200:203], v[58:61]
	v_mfma_f32_16x16x32_f16 v[66:69], v[136:139], v[208:211], v[66:69]
	v_mfma_f32_16x16x32_f16 v[78:81], v[136:139], v[212:215], v[78:81]
	v_mfma_f32_16x16x32_f16 v[70:73], v[136:139], v[216:219], v[70:73]
	s_waitcnt vmcnt(13)
	v_mfma_f32_16x16x32_f16 v[54:57], v[184:187], v[200:203], v[54:57]
	v_mfma_f32_16x16x32_f16 v[74:77], v[184:187], v[208:211], v[74:77]
	v_mfma_f32_16x16x32_f16 v[82:85], v[184:187], v[212:215], v[82:85]
	v_mfma_f32_16x16x32_f16 v[62:65], v[184:187], v[216:219], v[62:65]
	s_waitcnt vmcnt(12)
	v_mfma_f32_16x16x32_f16 v[38:41], v[204:207], v[200:203], v[38:41]
	buffer_load_dwordx4 v[126:129], v147, s[16:19], s8 offen
	buffer_load_dwordx4 v[136:139], v148, s[16:19], s8 offen
	buffer_load_dwordx4 v[184:187], v149, s[16:19], s8 offen
	buffer_load_dwordx4 v[200:203], v150, s[16:19], s8 offen
	v_mfma_f32_16x16x32_f16 v[42:45], v[204:207], v[208:211], v[42:45]
	v_mfma_f32_16x16x32_f16 v[46:49], v[204:207], v[212:215], v[46:49]
	v_mfma_f32_16x16x32_f16 v[34:37], v[204:207], v[216:219], v[34:37]
	v_add_u32_e32 v111, s76, v111
	ds_read_b128 v[204:207], v111
	ds_read_b128 v[208:211], v111 offset:16384
	ds_read_b128 v[212:215], v111 offset:32768
	ds_read_b128 v[216:219], v111 offset:49152
	s_add_i32 s8, s22, s45
	s_waitcnt vmcnt(15) lgkmcnt(7)
	v_mfma_f32_16x16x32_f16 v[164:167], v[94:97], v[176:179], v[164:167]
	s_waitcnt lgkmcnt(6)
	v_mfma_f32_16x16x32_f16 v[168:171], v[94:97], v[220:223], v[168:171]
	s_waitcnt vmcnt(14)
	v_mfma_f32_16x16x32_f16 v[58:61], v[122:125], v[176:179], v[58:61]
	v_mfma_f32_16x16x32_f16 v[66:69], v[122:125], v[220:223], v[66:69]
	s_waitcnt lgkmcnt(5)
	v_mfma_f32_16x16x32_f16 v[78:81], v[122:125], v[224:227], v[78:81]
	s_waitcnt lgkmcnt(4)
	v_mfma_f32_16x16x32_f16 v[70:73], v[122:125], v[228:231], v[70:73]
	s_waitcnt vmcnt(13)
	v_mfma_f32_16x16x32_f16 v[54:57], v[156:159], v[176:179], v[54:57]
	v_mfma_f32_16x16x32_f16 v[74:77], v[156:159], v[220:223], v[74:77]
	v_mfma_f32_16x16x32_f16 v[82:85], v[156:159], v[224:227], v[82:85]
	v_mfma_f32_16x16x32_f16 v[62:65], v[156:159], v[228:231], v[62:65]
	s_waitcnt vmcnt(12)
	v_mfma_f32_16x16x32_f16 v[38:41], v[180:183], v[176:179], v[38:41]
	v_mfma_f32_16x16x32_f16 v[42:45], v[180:183], v[220:223], v[42:45]
	buffer_load_dwordx4 v[122:125], v147, s[16:19], s8 offen
	buffer_load_dwordx4 v[156:159], v148, s[16:19], s8 offen
	buffer_load_dwordx4 v[176:179], v149, s[16:19], s8 offen
	buffer_load_dwordx4 v[220:223], v150, s[16:19], s8 offen
	v_mfma_f32_16x16x32_f16 v[50:53], v[94:97], v[228:231], v[50:53]
	v_mfma_f32_16x16x32_f16 v[46:49], v[180:183], v[224:227], v[46:49]
	v_mfma_f32_16x16x32_f16 v[34:37], v[180:183], v[228:231], v[34:37]
	v_mfma_f32_16x16x32_f16 v[172:175], v[94:97], v[224:227], v[172:175]
	v_add_u32_e32 v98, s77, v98
	ds_read_b128 v[94:97], v98
	ds_read_b128 v[180:183], v98 offset:16384
	ds_read_b128 v[224:227], v98 offset:32768
	ds_read_b128 v[228:231], v98 offset:49152
	s_add_i32 s8, s22, s46
	s_waitcnt vmcnt(15) lgkmcnt(7)
	v_mfma_f32_16x16x32_f16 v[164:167], v[90:93], v[204:207], v[164:167]
	s_waitcnt lgkmcnt(6)
	v_mfma_f32_16x16x32_f16 v[168:171], v[90:93], v[208:211], v[168:171]
	s_waitcnt lgkmcnt(5)
	v_mfma_f32_16x16x32_f16 v[172:175], v[90:93], v[212:215], v[172:175]
	s_waitcnt lgkmcnt(4)
	v_mfma_f32_16x16x32_f16 v[90:93], v[90:93], v[216:219], v[50:53]
	s_waitcnt vmcnt(14)
	v_mfma_f32_16x16x32_f16 v[232:235], v[188:191], v[204:207], v[58:61]
	v_mfma_f32_16x16x32_f16 v[66:69], v[188:191], v[208:211], v[66:69]
	v_mfma_f32_16x16x32_f16 v[78:81], v[188:191], v[212:215], v[78:81]
	v_mfma_f32_16x16x32_f16 v[70:73], v[188:191], v[216:219], v[70:73]
	s_waitcnt vmcnt(13)
	v_mfma_f32_16x16x32_f16 v[188:191], v[192:195], v[204:207], v[54:57]
	v_mfma_f32_16x16x32_f16 v[74:77], v[192:195], v[208:211], v[74:77]
	v_mfma_f32_16x16x32_f16 v[82:85], v[192:195], v[212:215], v[82:85]
	v_mfma_f32_16x16x32_f16 v[62:65], v[192:195], v[216:219], v[62:65]
	s_waitcnt vmcnt(12)
	v_mfma_f32_16x16x32_f16 v[192:195], v[196:199], v[204:207], v[38:41]
	buffer_load_dwordx4 v[58:61], v147, s[16:19], s8 offen
	buffer_load_dwordx4 v[54:57], v148, s[16:19], s8 offen
	buffer_load_dwordx4 v[50:53], v149, s[16:19], s8 offen
	buffer_load_dwordx4 v[38:41], v150, s[16:19], s8 offen
	v_mfma_f32_16x16x32_f16 v[42:45], v[196:199], v[208:211], v[42:45]
	v_mfma_f32_16x16x32_f16 v[46:49], v[196:199], v[212:215], v[46:49]
	v_mfma_f32_16x16x32_f16 v[196:199], v[196:199], v[216:219], v[34:37]
	v_add_u32_e32 v99, s78, v99
	ds_read_b128 v[204:207], v99
	ds_read_b128 v[208:211], v99 offset:16384
	ds_read_b128 v[212:215], v99 offset:32768
	ds_read_b128 v[216:219], v99 offset:49152
	s_add_i32 s8, s22, s47
	s_waitcnt vmcnt(15) lgkmcnt(7)
	v_mfma_f32_16x16x32_f16 v[164:167], v[86:89], v[94:97], v[164:167]
	s_waitcnt lgkmcnt(6)
	v_mfma_f32_16x16x32_f16 v[168:171], v[86:89], v[180:183], v[168:171]
	s_waitcnt lgkmcnt(5)
	v_mfma_f32_16x16x32_f16 v[172:175], v[86:89], v[224:227], v[172:175]
	s_waitcnt lgkmcnt(4)
	v_mfma_f32_16x16x32_f16 v[86:89], v[86:89], v[228:231], v[90:93]
	s_waitcnt vmcnt(14)
	v_mfma_f32_16x16x32_f16 v[232:235], v[140:143], v[94:97], v[232:235]
	v_mfma_f32_16x16x32_f16 v[66:69], v[140:143], v[180:183], v[66:69]
	v_mfma_f32_16x16x32_f16 v[236:239], v[140:143], v[224:227], v[78:81]
	v_mfma_f32_16x16x32_f16 v[70:73], v[140:143], v[228:231], v[70:73]
	s_waitcnt vmcnt(13)
	v_mfma_f32_16x16x32_f16 v[140:143], v[152:155], v[94:97], v[188:191]
	v_mfma_f32_16x16x32_f16 v[74:77], v[152:155], v[180:183], v[74:77]
	v_mfma_f32_16x16x32_f16 v[82:85], v[152:155], v[224:227], v[82:85]
	v_mfma_f32_16x16x32_f16 v[62:65], v[152:155], v[228:231], v[62:65]
	s_waitcnt vmcnt(12)
	v_mfma_f32_16x16x32_f16 v[152:155], v[160:163], v[94:97], v[192:195]
	buffer_load_dwordx4 v[94:97], v147, s[16:19], s8 offen
	buffer_load_dwordx4 v[90:93], v148, s[16:19], s8 offen
	buffer_load_dwordx4 v[78:81], v149, s[16:19], s8 offen
	buffer_load_dwordx4 v[34:37], v150, s[16:19], s8 offen
	v_mfma_f32_16x16x32_f16 v[42:45], v[160:163], v[180:183], v[42:45]
	v_mfma_f32_16x16x32_f16 v[46:49], v[160:163], v[224:227], v[46:49]
	v_mfma_f32_16x16x32_f16 v[160:163], v[160:163], v[228:231], v[196:199]
	v_add_u32_e32 v100, s79, v100
	ds_read_b128 v[180:183], v100
	ds_read_b128 v[188:191], v100 offset:16384
	ds_read_b128 v[192:195], v100 offset:32768
	ds_read_b128 v[196:199], v100 offset:49152
	s_add_i32 s8, s22, s48
	s_waitcnt vmcnt(15) lgkmcnt(7)
	v_mfma_f32_16x16x32_f16 v[164:167], v[126:129], v[204:207], v[164:167]
	s_waitcnt lgkmcnt(6)
	v_mfma_f32_16x16x32_f16 v[168:171], v[126:129], v[208:211], v[168:171]
	s_waitcnt lgkmcnt(5)
	v_mfma_f32_16x16x32_f16 v[172:175], v[126:129], v[212:215], v[172:175]
	s_waitcnt lgkmcnt(4)
	v_mfma_f32_16x16x32_f16 v[86:89], v[126:129], v[216:219], v[86:89]
	s_waitcnt vmcnt(14)
	v_mfma_f32_16x16x32_f16 v[126:129], v[136:139], v[204:207], v[232:235]
	v_mfma_f32_16x16x32_f16 v[66:69], v[136:139], v[208:211], v[66:69]
	v_mfma_f32_16x16x32_f16 v[224:227], v[136:139], v[212:215], v[236:239]
	v_mfma_f32_16x16x32_f16 v[136:139], v[136:139], v[216:219], v[70:73]
	s_waitcnt vmcnt(13)
	v_mfma_f32_16x16x32_f16 v[140:143], v[184:187], v[204:207], v[140:143]
	v_mfma_f32_16x16x32_f16 v[74:77], v[184:187], v[208:211], v[74:77]
	v_mfma_f32_16x16x32_f16 v[228:231], v[184:187], v[212:215], v[82:85]
	v_mfma_f32_16x16x32_f16 v[184:187], v[184:187], v[216:219], v[62:65]
	s_waitcnt vmcnt(12)
	v_mfma_f32_16x16x32_f16 v[152:155], v[200:203], v[204:207], v[152:155]
	v_mfma_f32_16x16x32_f16 v[204:207], v[200:203], v[208:211], v[42:45]
	buffer_load_dwordx4 v[82:85], v147, s[16:19], s8 offen
	buffer_load_dwordx4 v[70:73], v148, s[16:19], s8 offen
	buffer_load_dwordx4 v[62:65], v149, s[16:19], s8 offen
	buffer_load_dwordx4 v[42:45], v150, s[16:19], s8 offen
	v_mfma_f32_16x16x32_f16 v[46:49], v[200:203], v[212:215], v[46:49]
	v_mfma_f32_16x16x32_f16 v[160:163], v[200:203], v[216:219], v[160:163]
	v_add_u32_e32 v0, 0x1ac00, v104
	ds_read_b128 v[240:243], v0
	ds_read_b128 v[244:247], v0 offset:16
	s_waitcnt vmcnt(12) lgkmcnt(5)
	v_mfma_f32_16x16x32_f16 v[164:167], v[122:125], v[180:183], v[164:167]
	v_mfma_f32_16x16x32_f16 v[126:129], v[156:159], v[180:183], v[126:129]
	v_mfma_f32_16x16x32_f16 v[140:143], v[176:179], v[180:183], v[140:143]
	v_mfma_f32_16x16x32_f16 v[152:155], v[220:223], v[180:183], v[152:155]
	s_waitcnt lgkmcnt(4)
	v_mfma_f32_16x16x32_f16 v[168:171], v[122:125], v[188:191], v[168:171]
	v_mfma_f32_16x16x32_f16 v[208:211], v[156:159], v[188:191], v[66:69]
	v_mfma_f32_16x16x32_f16 v[212:215], v[176:179], v[188:191], v[74:77]
	v_mfma_f32_16x16x32_f16 v[204:207], v[220:223], v[188:191], v[204:207]
	s_waitcnt lgkmcnt(3)
	v_mfma_f32_16x16x32_f16 v[172:175], v[122:125], v[192:195], v[172:175]
	v_cvt_pk_f16_f32 v232, v164, v165
	v_cvt_pk_f16_f32 v233, v166, v167
	v_pk_max_f16 v232, v232, 0
	v_pk_max_f16 v233, v233, 0
	v_mfma_f32_16x16x32_f16 v[224:227], v[156:159], v[192:195], v[224:227]
	v_cvt_pk_f16_f32 v234, v126, v127
	v_cvt_pk_f16_f32 v235, v128, v129
	v_pk_max_f16 v234, v234, 0
	v_pk_max_f16 v235, v235, 0
	v_mfma_f32_16x16x32_f16 v[228:231], v[176:179], v[192:195], v[228:231]
	v_cvt_pk_f16_f32 v236, v140, v141
	v_cvt_pk_f16_f32 v237, v142, v143
	v_pk_max_f16 v236, v236, 0
	v_pk_max_f16 v237, v237, 0
	v_mfma_f32_16x16x32_f16 v[216:219], v[220:223], v[192:195], v[46:49]
	v_cvt_pk_f16_f32 v238, v152, v153
	v_cvt_pk_f16_f32 v239, v154, v155
	v_pk_max_f16 v238, v238, 0
	v_pk_max_f16 v239, v239, 0
	s_waitcnt lgkmcnt(2)
	v_mfma_f32_16x16x32_f16 v[200:203], v[122:125], v[196:199], v[86:89]
	v_cvt_pk_f16_f32 v180, v168, v169
	v_cvt_pk_f16_f32 v181, v170, v171
	v_pk_max_f16 v180, v180, 0
	v_pk_max_f16 v181, v181, 0
	s_add_i32 s8, s22, s49
	buffer_load_dwordx4 v[86:89], v147, s[16:19], s8 offen
	buffer_load_dwordx4 v[74:77], v148, s[16:19], s8 offen
	buffer_load_dwordx4 v[66:69], v149, s[16:19], s8 offen
	buffer_load_dwordx4 v[46:49], v150, s[16:19], s8 offen
	v_mfma_f32_16x16x32_f16 v[136:139], v[156:159], v[196:199], v[136:139]
	v_cvt_pk_f16_f32 v182, v208, v209
	v_cvt_pk_f16_f32 v183, v210, v211
	v_pk_max_f16 v182, v182, 0
	v_pk_max_f16 v183, v183, 0
	s_waitcnt lgkmcnt(1)
	v_mfma_f32_16x16x32_f16 v[252:255], v[240:243], v[232:235], 0
	v_cvt_pk_f16_f32 v232, v172, v173
	v_cvt_pk_f16_f32 v233, v174, v175
	v_pk_max_f16 v232, v232, 0
	v_pk_max_f16 v233, v233, 0
	v_mfma_f32_16x16x32_f16 v[184:187], v[176:179], v[196:199], v[184:187]
	v_cvt_pk_f16_f32 v188, v212, v213
	v_cvt_pk_f16_f32 v189, v214, v215
	v_pk_max_f16 v188, v188, 0
	v_pk_max_f16 v189, v189, 0
	s_waitcnt lgkmcnt(0)
	v_mfma_f32_16x16x32_f16 v[252:255], v[244:247], v[236:239], v[252:255]
	ds_read_u16 v102, v114
	ds_read_u16 v103, v114 offset:512
	ds_read_u16 v115, v114 offset:1024
	ds_read_u16 v116, v114 offset:1536
	v_cvt_pk_f16_f32 v234, v224, v225
	v_cvt_pk_f16_f32 v235, v226, v227
	v_pk_max_f16 v234, v234, 0
	v_pk_max_f16 v235, v235, 0
	v_mfma_f32_16x16x32_f16 v[160:163], v[220:223], v[196:199], v[160:163]
	v_cvt_pk_f16_f32 v190, v204, v205
	v_cvt_pk_f16_f32 v191, v206, v207
	v_pk_max_f16 v190, v190, 0
	v_pk_max_f16 v191, v191, 0
	v_mfma_f32_16x16x32_f16 v[192:195], v[240:243], v[180:183], 0
	v_cvt_pk_f16_f32 v236, v228, v229
	v_cvt_pk_f16_f32 v237, v230, v231
	v_pk_max_f16 v236, v236, 0
	v_pk_max_f16 v237, v237, 0
	v_mfma_f32_16x16x32_f16 v[192:195], v[244:247], v[188:191], v[192:195]
	v_cvt_pk_f16_f32 v238, v216, v217
	v_cvt_pk_f16_f32 v239, v218, v219
	v_pk_max_f16 v238, v238, 0
	v_pk_max_f16 v239, v239, 0
	v_cvt_pk_f16_f32 v180, v200, v201
	v_cvt_pk_f16_f32 v181, v202, v203
	v_pk_max_f16 v180, v180, 0
	v_pk_max_f16 v181, v181, 0
	v_mfma_f32_16x16x32_f16 v[196:199], v[240:243], v[232:235], 0
	v_cvt_pk_f16_f32 v182, v136, v137
	v_cvt_pk_f16_f32 v183, v138, v139
	v_pk_max_f16 v182, v182, 0
	v_pk_max_f16 v183, v183, 0
	v_mfma_f32_16x16x32_f16 v[196:199], v[244:247], v[236:239], v[196:199]
	v_cvt_pk_f16_f32 v188, v184, v185
	v_cvt_pk_f16_f32 v189, v186, v187
	v_pk_max_f16 v188, v188, 0
	v_pk_max_f16 v189, v189, 0
	v_cvt_pk_f16_f32 v190, v160, v161
	v_cvt_pk_f16_f32 v191, v162, v163
	v_pk_max_f16 v190, v190, 0
	v_pk_max_f16 v191, v191, 0
	v_mfma_f32_16x16x32_f16 v[122:125], v[240:243], v[180:183], 0
	s_nop 0
	v_mfma_f32_16x16x32_f16 v[122:125], v[244:247], v[188:191], v[122:125]
	v_add_u32_e32 v145, 0x12c00, v105
	ds_read_b128 v[240:243], v145 offset:2048
	ds_read_b128 v[244:247], v145 offset:2064
	ds_read_b128 v[248:251], v145 offset:2080
	s_load_dword s30, s[12:13], 0x0
	v_cndmask_b32_e64 v0, v252, v192, s[2:3]
	ds_read_b128 v[252:255], v145 offset:2096
	v_cndmask_b32_e64 v0, v0, v196, s[0:1]
	v_cndmask_b32_e64 v0, v0, v122, s[26:27]
	ds_write_b32 v112, v0
	s_waitcnt vmcnt(16)
	v_cndmask_b32_e64 v1, v30, v134, s[0:1]
	v_bfi_b32 v30, s10, v1, v30
	v_perm_b32 v1, v22, v134, s24
	v_cndmask_b32_e64 v22, v22, v1, s[0:1]
	v_bfi_b32 v1, s10, v135, v18
	v_perm_b32 v121, v10, v135, s24
	v_cndmask_b32_e64 v18, v18, v1, s[0:1]
	v_cndmask_b32_e64 v10, v10, v121, s[0:1]
	s_add_i32 s22, s22, 0x80000
	s_add_i32 s11, s11, 1
	s_add_u32 s12, s12, 4
	s_addc_u32 s13, s13, 0
	v_add_u32_e32 v104, 0x400, v104
	v_add_u32_e32 v105, 0x800, v105
	v_add_u32_e32 v114, 2, v114
	s_cmp_eq_u32 s22, 0x898000
	s_waitcnt lgkmcnt(0)
	s_barrier
	ds_read_b128 v[232:235], v113
	ds_read_b128 v[236:239], v113 offset:1024
	s_waitcnt lgkmcnt(0)
	v_add_f32_e32 v0, v232, v233
	v_add_f32_e32 v1, v234, v235
	v_add_f32_e32 v121, v236, v237
	v_add_f32_e32 v144, v238, v239
	v_add_f32_e32 v0, v0, v1
	v_add_f32_e32 v121, v121, v144
	v_add_f32_e32 v0, v0, v121
	v_add_f32_e32 v0, s30, v0
	ds_write_b32 v106, v0
	v_cvt_f16_f32_e32 v1, v0
	v_cvt_f16_f32_e32 v121, v0
	s_nop 1
	v_permlane16_swap_b32_e32 v1, v121
	v_mov_b32_e32 v144, v1
	v_mov_b32_e32 v145, v121
	s_nop 1
	v_permlane32_swap_b32_e32 v1, v144
	v_permlane32_swap_b32_e32 v121, v145
	v_add_u32_e32 v106, 4, v106
	s_cbranch_scc0 .LBB1_4
